# in-proj tile order with at most one sigmoid pair per round: r0 gelu|sigmoid, r1 gelu-stat|sigmoid, r2 plain|rope-q, r3 sigmoid|rope-k, r4 sigmoid
# speedup vs baseline: 1.0246x; 1.0246x over previous
;     __device__ bool next(int i, Unit& u) const { if (!base.next(i >> 1, u)) return false; if (i & 1) { u.pm += MTOK / BM; u.pn += DM / BM; } return true; }
;   __device__ __forceinline__ bool next(int i,AttnUnit&u)const{ if(i>=2||vcu>=256)return false; const int s=vcu&3; u.bh=vcu>>2; u.qb=(i==0)?7-s:s; return true; }
;     __host__ __device__ bool next(int i, Unit& u) const {
;         const int L = i * G + c; if (L >= nwg) return false;
;         int wgid = L; { const int q = nwg / NXCD, r = nwg % NXCD, xcd = wgid % NXCD, off = wgid / NXCD; wgid = (xcd < r ? xcd * (q + 1) : r * (q + 1) + (xcd - r) * q) + off; }
;         const int nig = WGM * nN, gid = wgid / nig, fm = gid * WGM, gsz = (nM - fm) < WGM ? (nM - fm) : WGM;
;         u.pm = fm + ((wgid % nig) % gsz); u.pn = (wgid % nig) / gsz; u.half = 0; return true;
.LBB0_382:
	s_ashr_i32 s4, s21, 31
	s_lshr_b32 s4, s4, 29
	s_add_i32 s4, s21, s4
	s_ashr_i32 s5, s4, 3
	s_and_b32 s4, s4, -8
	s_sub_i32 s4, s21, s4
	s_cmp_lt_i32 s4, 0
	s_movk_i32 s6, 0x91
	s_cselect_b32 s6, s6, 0x90
	s_mul_i32 s4, s4, s6
	s_add_i32 s4, s4, s5
	s_mul_hi_i32 s5, s4, 0x38e38e39
	s_lshr_b32 s6, s5, 31
	s_ashr_i32 s5, s5, 5
	s_add_i32 s5, s5, s6
	s_lshl_b32 s6, s5, 3
	s_mulk_i32 s5, 0x90
	s_sub_i32 s4, s4, s5
	s_bfe_u32 s5, s4, 0x3001c
	s_add_i32 s5, s4, s5
	s_sext_i32_i16 s7, s5
	s_and_b32 s5, s5, 0xfff8
	s_sub_i32 s4, s4, s5
	s_sext_i32_i16 s4, s4
	s_add_i32 s18, s6, s4
	s_ashr_i32 s70, s7, 3
	s_mul_i32 s4, s70, 5
	s_cmp_lt_u32 s70, 12
	s_cbranch_scc0 .Lpn_hi0
	s_mov_b32 s6, 0x625a820
	s_mov_b32 s7, 0x291286b
	s_branch .Lpn_go0
.Lpn_hi0:
	s_sub_i32 s4, s4, 60
	s_mov_b32 s6, 0x230399ee
	s_mov_b32 s7, 0

;     __device__ bool next(int i, Unit& u) const { if (!base.next(i >> 1, u)) return false; if (i & 1) { u.pm += MTOK / BM; u.pn += DM / BM; } return true; }
;   __device__ __forceinline__ bool next(int i,AttnUnit&u)const{ if(i>=2||vcu>=256)return false; const int s=vcu&3; u.bh=vcu>>2; u.qb=(i==0)?7-s:s; return true; }
;     __host__ __device__ bool next(int i, Unit& u) const {
;         const int L = i * G + c; if (L >= nwg) return false;
;         int wgid = L; { const int q = nwg / NXCD, r = nwg % NXCD, xcd = wgid % NXCD, off = wgid / NXCD; wgid = (xcd < r ? xcd * (q + 1) : r * (q + 1) + (xcd - r) * q) + off; }
;         const int nig = WGM * nN, gid = wgid / nig, fm = gid * WGM, gsz = (nM - fm) < WGM ? (nM - fm) : WGM;
;         u.pm = fm + ((wgid % nig) % gsz); u.pn = (wgid % nig) / gsz; u.half = 0; return true;
; template <class Epi, class Sched, bool ALIGN_EPI = false, bool SP2 = false>
; __device__ __forceinline__ void gemm_phase(PG8_LAS unsigned char* lds, const Gemm g, const Sched& S, const Epi& E) {
;     ...
;         const bool has_next = S.next(ui + 1, nxt);
;         const char* nA = has_next ? (const char*)g.A + (size_t)nxt.pm * tstep + (nxt.half == 2 ? hstep : (size_t)0) : cA; const char* nB = has_next ? (const char*)g.Bt + (size_t)nxt.pn * tstep : cB;
.LBB0_392:
	s_add_i32 s72, s72, 1
	s_mul_i32 s10, s72, s33
	s_add_i32 s10, s10, s21
	s_cmpk_lt_i32 s10, 0x480
	s_cselect_b64 s[64:65], -1, 0
	s_cmpk_gt_i32 s10, 0x47f
	s_cbranch_scc1 .LBB0_394
	s_ashr_i32 s11, s10, 31
	s_lshr_b32 s11, s11, 29
	s_add_i32 s11, s10, s11
	s_ashr_i32 s12, s11, 3
	s_and_b32 s11, s11, -8
	s_sub_i32 s10, s10, s11
	s_cmp_lt_i32 s10, 0
	s_movk_i32 s11, 0x91
	s_cselect_b32 s11, s11, 0x90
	s_mul_i32 s10, s10, s11
	s_add_i32 s10, s10, s12
	s_mul_hi_i32 s11, s10, 0x38e38e39
	s_lshr_b32 s12, s11, 31
	s_ashr_i32 s11, s11, 5
	s_add_i32 s11, s11, s12
	s_lshl_b32 s12, s11, 3
	s_mulk_i32 s11, 0x90
	s_sub_i32 s10, s10, s11
	s_bfe_u32 s11, s10, 0x3001c
	s_add_i32 s11, s10, s11
	s_sext_i32_i16 s13, s11
	s_and_b32 s11, s11, 0xfff8
	s_sub_i32 s10, s10, s11
	s_sext_i32_i16 s10, s10
	s_add_i32 s60, s12, s10
	s_ashr_i32 s62, s13, 3
	s_mul_i32 s10, s62, 5
	s_cmp_lt_u32 s62, 12
	s_cbranch_scc0 .Lpn_hi1
	s_mov_b32 s12, 0x625a820
	s_mov_b32 s13, 0x291286b
	s_branch .Lpn_go1
.Lpn_hi1:
	s_sub_i32 s10, s10, 60
	s_mov_b32 s12, 0x230399ee
	s_mov_b32 s13, 0
